# v027 plus grid barrier: XCD leader releases its XCD generation before its own acquire invalidate
# speedup vs baseline: 1.0024x; 1.0024x over previous
.LBB0_289:
	s_or_b64 exec, exec, s[6:7]
	s_mov_b64 s[6:7], exec
	v_mbcnt_lo_u32_b32 v1, s6, 0
	v_mbcnt_hi_u32_b32 v1, s7, v1
	v_cmp_eq_u32_e32 vcc, 0, v1
	s_waitcnt vmcnt(0)
	s_and_saveexec_b64 s[10:11], vcc
	s_cbranch_execz .LBB0_291
	s_bcnt1_i32_b64 s0, s[6:7]
	v_mov_b32_e32 v1, 0x2000
	v_mov_b32_e32 v2, s0
	global_atomic_add v1, v2, s[8:9] offset:1024
.LBB0_291:
	s_or_b64 exec, exec, s[10:11]
	buffer_inv sc1
	s_waitcnt vmcnt(0)

.LBB0_460:
	s_or_b64 exec, exec, s[8:9]
	s_mov_b64 s[8:9], exec
	v_mbcnt_lo_u32_b32 v1, s8, 0
	v_mbcnt_hi_u32_b32 v1, s9, v1
	v_cmp_eq_u32_e32 vcc, 0, v1
	s_waitcnt vmcnt(0)
	s_and_saveexec_b64 s[12:13], vcc
	s_cbranch_execz .LBB0_462
	s_bcnt1_i32_b64 s8, s[8:9]
	v_mov_b32_e32 v1, s8
	v_mov_b32_e32 v2, 0x2000
	global_atomic_add v2, v1, s[10:11] offset:1024
.LBB0_462:
	s_or_b64 exec, exec, s[12:13]
	buffer_inv sc1
	s_waitcnt vmcnt(0)

.LBB0_1477:
	s_or_b64 exec, exec, s[8:9]
	s_mov_b64 s[8:9], exec
	v_mbcnt_lo_u32_b32 v1, s8, 0
	v_mbcnt_hi_u32_b32 v1, s9, v1
	v_cmp_eq_u32_e32 vcc, 0, v1
	s_waitcnt vmcnt(0)
	s_and_saveexec_b64 s[14:15], vcc
	s_cbranch_execz .LBB0_1479
	s_bcnt1_i32_b64 s8, s[8:9]
	v_mov_b32_e32 v1, s8
	v_mov_b32_e32 v2, 0x2000
	global_atomic_add v2, v1, s[10:11] offset:1024
.LBB0_1479:
	s_or_b64 exec, exec, s[14:15]
	buffer_inv sc1
	s_waitcnt vmcnt(0)

.LBB0_1563:
	s_or_b64 exec, exec, s[10:11]
	s_mov_b64 s[10:11], exec
	v_mbcnt_lo_u32_b32 v1, s10, 0
	v_mbcnt_hi_u32_b32 v1, s11, v1
	v_cmp_eq_u32_e32 vcc, 0, v1
	s_waitcnt vmcnt(0)
	s_and_saveexec_b64 s[16:17], vcc
	s_cbranch_execz .LBB0_1565
	s_bcnt1_i32_b64 s10, s[10:11]
	v_mov_b32_e32 v1, s10
	v_mov_b32_e32 v2, 0x2000
	global_atomic_add v2, v1, s[14:15] offset:1024
.LBB0_1565:
	s_or_b64 exec, exec, s[16:17]
	buffer_inv sc1
	s_waitcnt vmcnt(0)

.LBB0_1683:
	s_or_b64 exec, exec, s[8:9]
	s_mov_b64 s[8:9], exec
	v_mbcnt_lo_u32_b32 v1, s8, 0
	v_mbcnt_hi_u32_b32 v1, s9, v1
	v_cmp_eq_u32_e32 vcc, 0, v1
	s_waitcnt vmcnt(0)
	s_and_saveexec_b64 s[14:15], vcc
	s_cbranch_execz .LBB0_1482
	s_bcnt1_i32_b64 s8, s[8:9]
	v_mov_b32_e32 v1, s8
	v_mov_b32_e32 v2, 0x2000
	global_atomic_add v2, v1, s[10:11] offset:1024
	s_branch .LBB0_1482

.LBB0_1832:
	s_or_b64 exec, exec, s[6:7]
	s_mov_b64 s[6:7], exec
	v_mbcnt_lo_u32_b32 v1, s6, 0
	v_mbcnt_hi_u32_b32 v1, s7, v1
	v_cmp_eq_u32_e32 vcc, 0, v1
	s_waitcnt vmcnt(0)
	s_and_saveexec_b64 s[10:11], vcc
	s_cbranch_execz .LBB0_1834
	s_bcnt1_i32_b64 s6, s[6:7]
	v_mov_b32_e32 v1, s6
	v_mov_b32_e32 v2, 0x2000
	global_atomic_add v2, v1, s[8:9] offset:1024

.LBB0_1912:
	s_or_b64 exec, exec, s[0:1]
	s_mov_b64 s[0:1], exec
	v_mbcnt_lo_u32_b32 v0, s0, 0
	v_mbcnt_hi_u32_b32 v0, s1, v0
	v_cmp_eq_u32_e32 vcc, 0, v0
	s_waitcnt vmcnt(0)
	s_and_saveexec_b64 s[6:7], vcc
	s_cbranch_execz .LBB0_1914
	s_bcnt1_i32_b64 s0, s[0:1]
	v_mov_b32_e32 v0, 0x2000
	v_mov_b32_e32 v1, s0
	global_atomic_add v0, v1, s[4:5] offset:1024
.LBB0_1914:
	s_or_b64 exec, exec, s[6:7]
	buffer_inv sc1
	s_waitcnt vmcnt(0)
